# silu(c) staging loads batched; hosted conversion block now runs under the routing query-tile load latency (on top of v8)
# speedup vs baseline: 1.0311x; 1.0070x over previous
.LBB0_10:
	global_load_dword v144, v[2:3], off
	v_lshl_add_u64 v[2:3], v[2:3], 0, s[12:13]
	global_load_dword v145, v[2:3], off
	v_lshl_add_u64 v[2:3], v[2:3], 0, s[12:13]
	global_load_dword v146, v[2:3], off
	v_lshl_add_u64 v[2:3], v[2:3], 0, s[12:13]
	global_load_dword v147, v[2:3], off
	v_lshl_add_u64 v[2:3], v[2:3], 0, s[12:13]
	global_load_dword v148, v[2:3], off
	v_lshl_add_u64 v[2:3], v[2:3], 0, s[12:13]
	global_load_dword v149, v[2:3], off
	v_lshl_add_u64 v[2:3], v[2:3], 0, s[12:13]
	global_load_dword v150, v[2:3], off
	v_lshl_add_u64 v[2:3], v[2:3], 0, s[12:13]
	global_load_dword v151, v[2:3], off
	s_waitcnt vmcnt(7)
	v_mul_f32_e32 v7, 0xbfb8aa3b, v144
	v_exp_f32_e32 v7, v7
	s_nop 0
	v_add_f32_e32 v7, 1.0, v7
	v_div_scale_f32 v9, s[16:17], v7, v7, v144
	v_rcp_f32_e32 v10, v9
	v_div_scale_f32 v11, vcc, v144, v7, v144
	v_fma_f32 v12, -v9, v10, 1.0
	v_fmac_f32_e32 v10, v12, v10
	v_mul_f32_e32 v12, v11, v10
	v_fma_f32 v13, -v9, v12, v11
	v_fmac_f32_e32 v12, v13, v10
	v_fma_f32 v9, -v9, v12, v11
	v_div_fmas_f32 v9, v9, v10, v12
	v_div_fixup_f32 v6, v9, v7, v144
	ds_write_b32 v5, v6
	s_waitcnt vmcnt(6)
	v_mul_f32_e32 v7, 0xbfb8aa3b, v145
	v_exp_f32_e32 v7, v7
	s_nop 0
	v_add_f32_e32 v7, 1.0, v7
	v_div_scale_f32 v9, s[16:17], v7, v7, v145
	v_rcp_f32_e32 v10, v9
	v_div_scale_f32 v11, vcc, v145, v7, v145
	v_fma_f32 v12, -v9, v10, 1.0
	v_fmac_f32_e32 v10, v12, v10
	v_mul_f32_e32 v12, v11, v10
	v_fma_f32 v13, -v9, v12, v11
	v_fmac_f32_e32 v12, v13, v10
	v_fma_f32 v9, -v9, v12, v11
	v_div_fmas_f32 v9, v9, v10, v12
	v_div_fixup_f32 v6, v9, v7, v145
	ds_write_b32 v5, v6 offset:2048
	s_waitcnt vmcnt(5)
	v_mul_f32_e32 v7, 0xbfb8aa3b, v146
	v_exp_f32_e32 v7, v7
	s_nop 0
	v_add_f32_e32 v7, 1.0, v7
	v_div_scale_f32 v9, s[16:17], v7, v7, v146
	v_rcp_f32_e32 v10, v9
	v_div_scale_f32 v11, vcc, v146, v7, v146
	v_fma_f32 v12, -v9, v10, 1.0
	v_fmac_f32_e32 v10, v12, v10
	v_mul_f32_e32 v12, v11, v10
	v_fma_f32 v13, -v9, v12, v11
	v_fmac_f32_e32 v12, v13, v10
	v_fma_f32 v9, -v9, v12, v11
	v_div_fmas_f32 v9, v9, v10, v12
	v_div_fixup_f32 v6, v9, v7, v146
	ds_write_b32 v5, v6 offset:4096
	s_waitcnt vmcnt(4)
	v_mul_f32_e32 v7, 0xbfb8aa3b, v147
	v_exp_f32_e32 v7, v7
	s_nop 0
	v_add_f32_e32 v7, 1.0, v7
	v_div_scale_f32 v9, s[16:17], v7, v7, v147
	v_rcp_f32_e32 v10, v9
	v_div_scale_f32 v11, vcc, v147, v7, v147
	v_fma_f32 v12, -v9, v10, 1.0
	v_fmac_f32_e32 v10, v12, v10
	v_mul_f32_e32 v12, v11, v10
	v_fma_f32 v13, -v9, v12, v11
	v_fmac_f32_e32 v12, v13, v10
	v_fma_f32 v9, -v9, v12, v11
	v_div_fmas_f32 v9, v9, v10, v12
	v_div_fixup_f32 v6, v9, v7, v147
	ds_write_b32 v5, v6 offset:6144
	s_waitcnt vmcnt(3)
	v_mul_f32_e32 v7, 0xbfb8aa3b, v148
	v_exp_f32_e32 v7, v7
	s_nop 0
	v_add_f32_e32 v7, 1.0, v7
	v_div_scale_f32 v9, s[16:17], v7, v7, v148
	v_rcp_f32_e32 v10, v9
	v_div_scale_f32 v11, vcc, v148, v7, v148
	v_fma_f32 v12, -v9, v10, 1.0
	v_fmac_f32_e32 v10, v12, v10
	v_mul_f32_e32 v12, v11, v10
	v_fma_f32 v13, -v9, v12, v11
	v_fmac_f32_e32 v12, v13, v10
	v_fma_f32 v9, -v9, v12, v11
	v_div_fmas_f32 v9, v9, v10, v12
	v_div_fixup_f32 v6, v9, v7, v148
	ds_write_b32 v5, v6 offset:8192
	s_waitcnt vmcnt(2)
	v_mul_f32_e32 v7, 0xbfb8aa3b, v149
	v_exp_f32_e32 v7, v7
	s_nop 0
	v_add_f32_e32 v7, 1.0, v7
	v_div_scale_f32 v9, s[16:17], v7, v7, v149
	v_rcp_f32_e32 v10, v9
	v_div_scale_f32 v11, vcc, v149, v7, v149
	v_fma_f32 v12, -v9, v10, 1.0
	v_fmac_f32_e32 v10, v12, v10
	v_mul_f32_e32 v12, v11, v10
	v_fma_f32 v13, -v9, v12, v11
	v_fmac_f32_e32 v12, v13, v10
	v_fma_f32 v9, -v9, v12, v11
	v_div_fmas_f32 v9, v9, v10, v12
	v_div_fixup_f32 v6, v9, v7, v149
	ds_write_b32 v5, v6 offset:10240
	s_waitcnt vmcnt(1)
	v_mul_f32_e32 v7, 0xbfb8aa3b, v150
	v_exp_f32_e32 v7, v7
	s_nop 0
	v_add_f32_e32 v7, 1.0, v7
	v_div_scale_f32 v9, s[16:17], v7, v7, v150
	v_rcp_f32_e32 v10, v9
	v_div_scale_f32 v11, vcc, v150, v7, v150
	v_fma_f32 v12, -v9, v10, 1.0
	v_fmac_f32_e32 v10, v12, v10
	v_mul_f32_e32 v12, v11, v10
	v_fma_f32 v13, -v9, v12, v11
	v_fmac_f32_e32 v12, v13, v10
	v_fma_f32 v9, -v9, v12, v11
	v_div_fmas_f32 v9, v9, v10, v12
	v_div_fixup_f32 v6, v9, v7, v150
	ds_write_b32 v5, v6 offset:12288
	s_waitcnt vmcnt(0)
	v_mul_f32_e32 v7, 0xbfb8aa3b, v151
	v_exp_f32_e32 v7, v7
	s_nop 0
	v_add_f32_e32 v7, 1.0, v7
	v_div_scale_f32 v9, s[16:17], v7, v7, v151
	v_rcp_f32_e32 v10, v9
	v_div_scale_f32 v11, vcc, v151, v7, v151
	v_fma_f32 v12, -v9, v10, 1.0
	v_fmac_f32_e32 v10, v12, v10
	v_mul_f32_e32 v12, v11, v10
	v_fma_f32 v13, -v9, v12, v11
	v_fmac_f32_e32 v12, v13, v10
	v_fma_f32 v9, -v9, v12, v11
	v_div_fmas_f32 v9, v9, v10, v12
	v_div_fixup_f32 v6, v9, v7, v151
	ds_write_b32 v5, v6 offset:14336

.LBB0_1809:
	s_lshl_b32 s56, s47, 5
	v_add_u32_e32 v2, s56, v72
	v_ashrrev_i32_e32 v3, 31, v2
	v_lshlrev_b64 v[2:3], 12, v[2:3]
	v_lshl_add_u64 v[10:11], v[38:39], 0, v[2:3]
	s_waitcnt lgkmcnt(0)
	s_barrier
	global_load_dwordx4 v[2:5], v[10:11], off
	global_load_dwordx4 v[6:9], v[10:11], off offset:16
	s_waitcnt vmcnt(2) lgkmcnt(0)
	s_mov_b32 s60, s96
	s_mov_b32 s61, s97
	s_mov_b64 s[66:67], s[98:99]
	s_mov_b64 s[68:69], s[96:97]
	s_mov_b64 s[70:71], s[98:99]
	s_movk_i32 s72, 0x1000
	s_movk_i32 s73, 0x3fff
	s_movk_i32 s74, 0x2000
	s_movk_i32 s75, 0x3000
	s_mov_b32 s76, 0xf800000
	s_mov_b32 s77, 0x8080808
	s_mov_b32 s78, 0x400000
	s_mov_b32 s79, 0x800000
	s_mov_b32 s80, 0xc00000
	s_mov_b32 s81, 0x1000000
	v_cmp_eq_u32_e64 s[82:83], 0, v1
	s_mov_b64 s[86:87], exec
	v_mul_f32_e32 v202, v207, v207
	v_mul_f32_e32 v203, v209, v209
	v_max_f32_e64 v204, |v207|, |v207|
	v_max_f32_e64 v205, |v206|, |v206|
	v_max_f32_e64 v214, |v209|, |v209|
	v_max_f32_e64 v215, |v208|, |v208|
	s_nop 0
	v_mul_f32_e32 v216, v191, v191
	v_mul_f32_e32 v217, v193, v193
	s_nop 0
	v_mul_f32_e32 v229, v187, v187
	v_mul_f32_e32 v235, v189, v189
	v_fmac_f32_e32 v202, v206, v206
	v_fmac_f32_e32 v203, v208, v208
	v_max_f32_e32 v204, v205, v204
	v_max_f32_e32 v205, v215, v214
	v_fmac_f32_e32 v216, v190, v190
	v_fmac_f32_e32 v217, v192, v192
	v_max_f32_e64 v218, |v191|, |v191|
	v_max_f32_e64 v219, |v190|, |v190|
	v_max_f32_e64 v236, |v187|, |v187|
	v_max_f32_e64 v237, |v186|, |v186|
	s_nop 0
	v_mul_f32_e32 v240, v179, v179
	v_mul_f32_e32 v241, v181, v181
	v_fmac_f32_e32 v229, v186, v186
	v_fmac_f32_e32 v235, v188, v188
	v_add_f32_e32 v202, v202, v203
	v_max3_f32 v203, v204, 0, v205
	v_add_f32_e32 v204, v216, v217
	v_max_f32_e32 v214, v219, v218
	v_max_f32_e32 v218, v237, v236
	v_fmac_f32_e32 v240, v178, v178
	v_fmac_f32_e32 v241, v180, v180
	s_nop 0
	v_mul_f32_e32 v236, v183, v183
	v_mul_f32_e32 v237, v185, v185
	v_add_f32_e32 v205, v229, v235
	v_add_f32_e32 v202, v202, v204
	v_max_f32_e64 v220, |v193|, |v193|
	v_max_f32_e64 v221, |v192|, |v192|
	v_add_f32_e32 v216, v240, v241
	v_fmac_f32_e32 v236, v182, v182
	v_fmac_f32_e32 v237, v184, v184
	v_add_f32_e32 v202, v202, v205
	v_max_f32_e64 v238, |v189|, |v189|
	v_max_f32_e64 v239, |v188|, |v188|
	v_max_f32_e32 v215, v221, v220
	v_add_f32_e32 v202, v202, v216
	v_add_f32_e32 v204, v236, v237
	v_max_f32_e64 v242, |v179|, |v179|
	v_max_f32_e64 v243, |v178|, |v178|
	v_max_f32_e64 v244, |v181|, |v181|
	v_max_f32_e64 v245, |v180|, |v180|
	v_max_f32_e32 v219, v239, v238
	v_max3_f32 v203, v203, v214, v215
	v_add_f32_e32 v202, v202, v204
	v_max_f32_e64 v204, |v183|, |v183|
	v_max_f32_e64 v205, |v182|, |v182|
	v_max_f32_e32 v220, v243, v242
	v_max_f32_e32 v221, v245, v244
	v_max3_f32 v203, v203, v218, v219
	v_max_f32_e32 v204, v205, v204
	v_max_f32_e64 v205, |v185|, |v185|
	v_max_f32_e64 v214, |v184|, |v184|
	v_max3_f32 v203, v203, v220, v221
	v_max_f32_e32 v205, v214, v205
	v_max3_f32 v203, v203, v204, v205
	v_mov_b32_e32 v218, v86
	v_mov_b32_e32 v219, v87
	v_mov_b32_e32 v220, v88
	v_mov_b32_e32 v221, v89
	v_mov_b32_e32 v214, v90
	v_mov_b32_e32 v215, v91
	v_mov_b32_e32 v216, v92
	v_mov_b32_e32 v217, v93
	v_cmp_lt_i32_e32 vcc, v157, v154
	s_nop 0
	v_mul_f32_e32 v204, v171, v171
	v_mul_f32_e32 v194, v173, v173
	v_fmac_f32_e32 v204, v170, v170
	v_fmac_f32_e32 v194, v172, v172
	v_add_f32_e32 v194, v204, v194
	v_add_f32_e32 v194, v202, v194
	v_max_f32_e64 v195, |v171|, |v171|
	v_max_f32_e64 v202, |v170|, |v170|
	v_max_f32_e32 v195, v202, v195
	v_max_f32_e64 v202, |v173|, |v173|
	v_max_f32_e64 v204, |v172|, |v172|
	v_max_f32_e32 v202, v204, v202
	v_max3_f32 v195, v203, v195, v202
	s_nop 0
	v_mul_f32_e32 v202, v223, v223
	v_mul_f32_e32 v203, v225, v225
	v_fmac_f32_e32 v202, v222, v222
	v_fmac_f32_e32 v203, v224, v224
	v_add_f32_e32 v202, v202, v203
	v_add_f32_e32 v194, v194, v202
	v_max_f32_e64 v202, |v223|, |v223|
	v_max_f32_e64 v203, |v222|, |v222|
	v_max_f32_e32 v202, v203, v202
	v_max_f32_e64 v203, |v225|, |v225|
	v_max_f32_e64 v204, |v224|, |v224|
	v_max_f32_e32 v203, v204, v203
	v_max3_f32 v229, v195, v202, v203
	v_mov_b32_e32 v202, v94
	v_mov_b32_e32 v203, v95
	v_mov_b32_e32 v204, v96
	v_mov_b32_e32 v205, v97
	s_nop 0
	v_mul_f32_e32 v195, v211, v211
	v_mul_f32_e32 v235, v213, v213
	v_fmac_f32_e32 v195, v210, v210
	v_fmac_f32_e32 v235, v212, v212
	v_add_f32_e32 v195, v195, v235
	v_add_f32_e32 v235, v194, v195
	v_max_f32_e64 v194, |v211|, |v211|
	v_max_f32_e64 v195, |v210|, |v210|
	v_max_f32_e32 v236, v195, v194
	v_max_f32_e64 v194, |v213|, |v213|
	v_max_f32_e64 v195, |v212|, |v212|
	v_max_f32_e32 v237, v195, v194
	v_mov_b32_e32 v194, v98
	v_mov_b32_e32 v195, v99
	v_mov_b32_e32 v196, v100
	v_mov_b32_e32 v197, v101
	v_max3_f32 v229, v229, v236, v237
	s_nop 0
	v_mul_f32_e32 v236, v199, v199
	v_mul_f32_e32 v237, v201, v201
	v_fmac_f32_e32 v236, v198, v198
	v_fmac_f32_e32 v237, v200, v200
	v_add_f32_e32 v236, v236, v237
	v_add_f32_e32 v235, v235, v236
	v_max_f32_e64 v236, |v199|, |v199|
	v_max_f32_e64 v237, |v198|, |v198|
	v_max_f32_e32 v236, v237, v236
	v_max_f32_e64 v237, |v201|, |v201|
	v_max_f32_e64 v238, |v200|, |v200|
	v_max_f32_e32 v237, v238, v237
	v_max3_f32 v229, v229, v236, v237
	s_nop 0
	v_mul_f32_e32 v236, v175, v175
	v_mul_f32_e32 v237, v177, v177
	v_fmac_f32_e32 v236, v174, v174
	v_fmac_f32_e32 v237, v176, v176
	v_add_f32_e32 v236, v236, v237
	v_add_f32_e32 v235, v235, v236
	v_max_f32_e64 v236, |v175|, |v175|
	v_max_f32_e64 v237, |v174|, |v174|
	v_max_f32_e32 v236, v237, v236
	v_max_f32_e64 v237, |v177|, |v177|
	v_max_f32_e64 v238, |v176|, |v176|
	v_max_f32_e32 v237, v238, v237
	v_max3_f32 v229, v229, v236, v237
	s_nop 0
	v_mul_f32_e32 v236, v167, v167
	v_mul_f32_e32 v237, v169, v169
	v_fmac_f32_e32 v236, v166, v166
	v_fmac_f32_e32 v237, v168, v168
	v_add_f32_e32 v236, v236, v237
	v_add_f32_e32 v235, v235, v236
	v_max_f32_e64 v236, |v167|, |v167|
	v_max_f32_e64 v237, |v166|, |v166|
	v_max_f32_e32 v236, v237, v236
	v_max_f32_e64 v237, |v169|, |v169|
	v_max_f32_e64 v238, |v168|, |v168|
	v_max_f32_e32 v237, v238, v237
	v_max3_f32 v229, v229, v236, v237
	s_nop 0
	v_mul_f32_e32 v236, v219, v219
	v_mul_f32_e32 v237, v221, v221
	v_fmac_f32_e32 v236, v218, v218
	v_fmac_f32_e32 v237, v220, v220
	v_add_f32_e32 v236, v236, v237
	v_add_f32_e32 v235, v235, v236
	v_max_f32_e64 v236, |v219|, |v219|
	v_max_f32_e64 v237, |v218|, |v218|
	v_max_f32_e32 v236, v237, v236
	v_max_f32_e64 v237, |v221|, |v221|
	v_max_f32_e64 v238, |v220|, |v220|
	v_max_f32_e32 v237, v238, v237
	v_max3_f32 v229, v229, v236, v237
	s_nop 0
	v_mul_f32_e32 v236, v215, v215
	v_mul_f32_e32 v237, v217, v217
	v_fmac_f32_e32 v236, v214, v214
	v_fmac_f32_e32 v237, v216, v216
	v_add_f32_e32 v236, v236, v237
	v_add_f32_e32 v235, v235, v236
	v_max_f32_e64 v236, |v215|, |v215|
	v_max_f32_e64 v237, |v214|, |v214|
	v_max_f32_e32 v236, v237, v236
	v_max_f32_e64 v237, |v217|, |v217|
	v_max_f32_e64 v238, |v216|, |v216|
	v_max_f32_e32 v237, v238, v237
	v_max3_f32 v229, v229, v236, v237
	s_nop 0
	v_mul_f32_e32 v236, v203, v203
	v_mul_f32_e32 v237, v205, v205
	v_fmac_f32_e32 v236, v202, v202
	v_fmac_f32_e32 v237, v204, v204
	v_add_f32_e32 v236, v236, v237
	v_add_f32_e32 v235, v235, v236
	v_max_f32_e64 v236, |v203|, |v203|
	v_max_f32_e64 v237, |v202|, |v202|
	v_max_f32_e32 v236, v237, v236
	v_max_f32_e64 v237, |v205|, |v205|
	v_max_f32_e64 v238, |v204|, |v204|
	v_max_f32_e32 v237, v238, v237
	v_max3_f32 v229, v229, v236, v237
	s_nop 0
	v_mul_f32_e32 v236, v195, v195
	v_mul_f32_e32 v237, v197, v197
	v_fmac_f32_e32 v236, v194, v194
	v_fmac_f32_e32 v237, v196, v196
	v_add_f32_e32 v236, v236, v237
	v_add_f32_e32 v235, v235, v236
	v_max_f32_e64 v236, |v195|, |v195|
	v_max_f32_e64 v237, |v194|, |v194|
	v_max_f32_e32 v236, v237, v236
	v_max_f32_e64 v237, |v197|, |v197|
	v_max_f32_e64 v238, |v196|, |v196|
	v_max_f32_e32 v237, v238, v237
	v_max3_f32 v229, v229, v236, v237
	v_mul_f32_e32 v236, v163, v163
	v_mul_f32_e32 v237, v165, v165
	v_fmac_f32_e32 v236, v162, v162
	v_fmac_f32_e32 v237, v164, v164
	v_add_f32_e32 v236, v236, v237
	v_add_f32_e32 v235, v235, v236
	v_max_f32_e64 v236, |v163|, |v163|
	v_max_f32_e64 v237, |v162|, |v162|
	v_max_f32_e32 v236, v237, v236
	v_max_f32_e64 v237, |v165|, |v165|
	v_max_f32_e64 v240, |v164|, |v164|
	v_cndmask_b32_e32 v238, v1, v157, vcc
	v_max_f32_e32 v237, v240, v237
	v_lshlrev_b32_e32 v238, 2, v238
	v_max3_f32 v229, v229, v236, v237
	ds_bpermute_b32 v239, v238, v235
	ds_bpermute_b32 v236, v238, v229
	v_cmp_lt_i32_e32 vcc, v158, v154
	s_waitcnt lgkmcnt(1)
	v_add_f32_e32 v235, v235, v239
	v_cndmask_b32_e32 v237, v1, v158, vcc
	v_lshlrev_b32_e32 v237, 2, v237
	s_waitcnt lgkmcnt(0)
	v_max_f32_e32 v236, v236, v236
	ds_bpermute_b32 v238, v237, v235
	v_max_f32_e32 v229, v229, v236
	ds_bpermute_b32 v236, v237, v229
	v_cmp_lt_i32_e32 vcc, v159, v154
	s_waitcnt lgkmcnt(1)
	v_add_f32_e32 v235, v235, v238
	v_cndmask_b32_e32 v237, v1, v159, vcc
	v_lshlrev_b32_e32 v237, 2, v237
	ds_bpermute_b32 v238, v237, v235
	s_waitcnt lgkmcnt(1)
	v_max_f32_e32 v236, v236, v236
	v_max_f32_e32 v229, v229, v236
	ds_bpermute_b32 v236, v237, v229
	v_cmp_lt_i32_e32 vcc, v160, v154
	s_waitcnt lgkmcnt(1)
	v_add_f32_e32 v235, v235, v238
	s_waitcnt lgkmcnt(0)
	v_max_f32_e32 v236, v236, v236
	v_cndmask_b32_e32 v237, v1, v160, vcc
	v_lshlrev_b32_e32 v237, 2, v237
	ds_bpermute_b32 v238, v237, v235
	v_max_f32_e32 v229, v229, v236
	ds_bpermute_b32 v236, v237, v229
	v_cmp_lt_i32_e32 vcc, v156, v154
	s_waitcnt lgkmcnt(1)
	v_add_f32_e32 v235, v235, v238
	v_cndmask_b32_e32 v237, v1, v156, vcc
	v_lshlrev_b32_e32 v237, 2, v237
	ds_bpermute_b32 v238, v237, v235
	s_waitcnt lgkmcnt(1)
	v_max_f32_e32 v236, v236, v236
	v_max_f32_e32 v229, v229, v236
	v_cmp_lt_i32_e32 vcc, v155, v154
	ds_bpermute_b32 v236, v237, v229
	s_waitcnt lgkmcnt(1)
	v_add_f32_e32 v235, v235, v238
	v_cndmask_b32_e32 v237, v1, v155, vcc
	v_lshlrev_b32_e32 v237, 2, v237
	ds_bpermute_b32 v238, v237, v235
	s_waitcnt lgkmcnt(1)
	v_max_f32_e32 v236, v236, v236
	v_max_f32_e32 v229, v229, v236
	ds_bpermute_b32 v236, v237, v229
	s_waitcnt lgkmcnt(1)
	v_add_f32_e32 v235, v235, v238
	v_mul_f32_e32 v235, 0x39800000, v235
	v_mul_f32_e32 v237, 0x4f800000, v235
	v_cmp_gt_f32_e32 vcc, s76, v235
	s_waitcnt lgkmcnt(0)
	v_max_f32_e32 v236, v236, v236
	v_max_f32_e32 v229, v229, v236
	v_cndmask_b32_e32 v235, v235, v237, vcc
	v_sqrt_f32_e32 v237, v235
	v_mul_f32_e32 v229, 0x3e088889, v229
	v_add_u32_e32 v236, -1, v237
	v_fma_f32 v238, -v236, v237, v235
	v_cmp_ge_f32_e64 s[88:89], 0, v238
	v_add_u32_e32 v238, 1, v237
	s_nop 0
	v_cndmask_b32_e64 v236, v237, v236, s[88:89]
	v_fma_f32 v237, -v238, v237, v235
	v_cmp_lt_f32_e64 s[88:89], 0, v237
	s_nop 1
	v_cndmask_b32_e64 v236, v236, v238, s[88:89]
	v_mul_f32_e32 v237, 0x37800000, v236
	v_cndmask_b32_e32 v236, v236, v237, vcc
	v_cmp_class_f32_e32 vcc, v235, v233
	s_nop 1
	v_cndmask_b32_e32 v235, v236, v235, vcc
	v_mul_f32_e32 v235, 0x3eab9f56, v235
	v_min_f32_e32 v229, v235, v229
	v_max_f32_e32 v235, 0xda24260, v229
	v_div_scale_f32 v229, s[88:89], v235, v235, 1.0
	v_rcp_f32_e32 v236, v229
	s_nop 0
	v_fma_f32 v237, -v229, v236, 1.0
	v_fmac_f32_e32 v236, v237, v236
	v_div_scale_f32 v237, vcc, 1.0, v235, 1.0
	v_mul_f32_e32 v238, v237, v236
	v_fma_f32 v239, -v229, v238, v237
	v_fmac_f32_e32 v238, v239, v236
	v_fma_f32 v229, -v229, v238, v237
	v_div_fmas_f32 v229, v229, v236, v238
	v_div_fixup_f32 v229, v229, v235, 1.0
	v_mul_f32_e32 v179, v179, v229
	v_mul_f32_e32 v178, v178, v229
	v_floor_f32_e32 v179, v179
	v_mul_f32_e32 v180, v180, v229
	v_floor_f32_e32 v178, v178
	v_add_f32_e32 v179, 0x41000000, v179
	v_floor_f32_e32 v180, v180
	v_add_f32_e32 v178, 0x41000000, v178
	v_med3_f32 v179, v179, 0, v234
	v_add_f32_e32 v180, 0x41000000, v180
	v_med3_f32 v178, v178, 0, v234
	v_cvt_i32_f32_e32 v179, v179
	v_med3_f32 v180, v180, 0, v234
	v_cvt_i32_f32_e32 v178, v178
	v_cvt_i32_f32_sdwa v180, v180 dst_sel:WORD_1 dst_unused:UNUSED_PAD src0_sel:DWORD
	v_lshlrev_b32_e32 v179, 8, v179
	v_mul_f32_e32 v171, v171, v229
	v_mul_f32_e32 v170, v170, v229
	v_or3_b32 v178, v179, v178, v180
	v_mul_f32_e32 v179, v181, v229
	v_mul_f32_e32 v181, v183, v229
	v_floor_f32_e32 v179, v179
	v_mul_f32_e32 v180, v182, v229
	v_floor_f32_e32 v181, v181
	v_mul_f32_e32 v182, v184, v229
	v_add_f32_e32 v179, 0x41000000, v179
	v_floor_f32_e32 v180, v180
	v_add_f32_e32 v181, 0x41000000, v181
	v_floor_f32_e32 v182, v182
	v_mul_f32_e32 v183, v185, v229
	v_floor_f32_e32 v171, v171
	v_mul_f32_e32 v172, v172, v229
	v_med3_f32 v179, v179, 0, v234
	v_add_f32_e32 v180, 0x41000000, v180
	v_med3_f32 v181, v181, 0, v234
	v_add_f32_e32 v182, 0x41000000, v182
	v_floor_f32_e32 v183, v183
	v_floor_f32_e32 v170, v170
	v_add_f32_e32 v171, 0x41000000, v171
	v_floor_f32_e32 v172, v172
	v_mul_f32_e32 v175, v175, v229
	v_cvt_i32_f32_sdwa v179, v179 dst_sel:BYTE_3 dst_unused:UNUSED_PAD src0_sel:DWORD
	v_med3_f32 v180, v180, 0, v234
	v_cvt_i32_f32_e32 v181, v181
	v_med3_f32 v182, v182, 0, v234
	v_add_f32_e32 v183, 0x41000000, v183
	v_add_f32_e32 v170, 0x41000000, v170
	v_med3_f32 v171, v171, 0, v234
	v_add_f32_e32 v172, 0x41000000, v172
	v_mul_f32_e32 v174, v174, v229
	v_floor_f32_e32 v175, v175
	v_mul_f32_e32 v176, v176, v229
	v_cvt_i32_f32_e32 v180, v180
	v_cvt_i32_f32_sdwa v182, v182 dst_sel:WORD_1 dst_unused:UNUSED_PAD src0_sel:DWORD
	v_med3_f32 v183, v183, 0, v234
	v_med3_f32 v170, v170, 0, v234
	v_cvt_i32_f32_e32 v171, v171
	v_med3_f32 v172, v172, 0, v234
	v_floor_f32_e32 v174, v174
	v_add_f32_e32 v175, 0x41000000, v175
	v_floor_f32_e32 v176, v176
	v_cvt_i32_f32_sdwa v183, v183 dst_sel:BYTE_3 dst_unused:UNUSED_PAD src0_sel:DWORD
	v_cvt_i32_f32_e32 v170, v170
	v_cvt_i32_f32_sdwa v172, v172 dst_sel:WORD_1 dst_unused:UNUSED_PAD src0_sel:DWORD
	v_add_f32_e32 v174, 0x41000000, v174
	v_med3_f32 v175, v175, 0, v234
	v_add_f32_e32 v176, 0x41000000, v176
	v_med3_f32 v174, v174, 0, v234
	v_cvt_i32_f32_e32 v175, v175
	v_med3_f32 v176, v176, 0, v234
	v_bitop3_b32 v178, v178, s77, v179 bitop3:0x36
	v_lshlrev_b32_e32 v179, 8, v181
	v_cvt_i32_f32_e32 v174, v174
	v_cvt_i32_f32_sdwa v176, v176 dst_sel:WORD_1 dst_unused:UNUSED_PAD src0_sel:DWORD
	v_or3_b32 v179, v179, v180, v182
	v_lshlrev_b32_e32 v171, 8, v171
	v_or_b32_e32 v180, v179, v183
	v_bitop3_b32 v179, v179, s77, v183 bitop3:0x36
	v_or3_b32 v170, v171, v170, v172
	v_mul_f32_e32 v171, v173, v229
	v_mul_f32_e32 v173, v223, v229
	v_cndmask_b32_e64 v179, v179, v180, s[86:87]
	v_floor_f32_e32 v171, v171
	v_mul_f32_e32 v172, v222, v229
	v_floor_f32_e32 v173, v173
	v_mul_f32_e32 v180, v224, v229
	v_lshlrev_b32_e32 v175, 8, v175
	v_add_f32_e32 v171, 0x41000000, v171
	v_floor_f32_e32 v172, v172
	v_add_f32_e32 v173, 0x41000000, v173
	v_floor_f32_e32 v180, v180
	v_or3_b32 v174, v175, v174, v176
	v_mul_f32_e32 v175, v177, v229
	v_mul_f32_e32 v167, v167, v229
	v_med3_f32 v171, v171, 0, v234
	v_add_f32_e32 v172, 0x41000000, v172
	v_med3_f32 v173, v173, 0, v234
	v_add_f32_e32 v180, 0x41000000, v180
	v_floor_f32_e32 v175, v175
	v_mul_f32_e32 v166, v166, v229
	v_floor_f32_e32 v167, v167
	v_mul_f32_e32 v168, v168, v229
	v_cvt_i32_f32_sdwa v171, v171 dst_sel:BYTE_3 dst_unused:UNUSED_PAD src0_sel:DWORD
	v_med3_f32 v172, v172, 0, v234
	v_cvt_i32_f32_e32 v173, v173
	v_med3_f32 v180, v180, 0, v234
	v_add_f32_e32 v175, 0x41000000, v175
	v_floor_f32_e32 v166, v166
	v_add_f32_e32 v167, 0x41000000, v167
	v_floor_f32_e32 v168, v168
	v_cvt_i32_f32_e32 v172, v172
	v_cvt_i32_f32_sdwa v180, v180 dst_sel:WORD_1 dst_unused:UNUSED_PAD src0_sel:DWORD
	v_med3_f32 v175, v175, 0, v234
	v_add_f32_e32 v166, 0x41000000, v166
	v_med3_f32 v167, v167, 0, v234
	v_add_f32_e32 v168, 0x41000000, v168
	v_cvt_i32_f32_sdwa v175, v175 dst_sel:BYTE_3 dst_unused:UNUSED_PAD src0_sel:DWORD
	v_med3_f32 v166, v166, 0, v234
	v_cvt_i32_f32_e32 v167, v167
	v_med3_f32 v168, v168, 0, v234
	v_cvt_i32_f32_e32 v166, v166
	v_cvt_i32_f32_sdwa v168, v168 dst_sel:WORD_1 dst_unused:UNUSED_PAD src0_sel:DWORD
	v_mul_f32_e32 v181, v225, v229
	v_bitop3_b32 v170, v170, s77, v171 bitop3:0x36
	v_lshlrev_b32_e32 v171, 8, v173
	v_floor_f32_e32 v181, v181
	v_or3_b32 v171, v171, v172, v180
	v_mul_f32_e32 v180, v211, v229
	v_mul_f32_e32 v169, v169, v229
	v_add_f32_e32 v181, 0x41000000, v181
	v_mul_f32_e32 v173, v210, v229
	v_floor_f32_e32 v180, v180
	v_mul_f32_e32 v182, v212, v229
	v_floor_f32_e32 v169, v169
	v_bitop3_b32 v174, v174, s77, v175 bitop3:0x36
	v_lshlrev_b32_e32 v167, 8, v167
	v_mul_f32_e32 v175, v219, v229
	v_med3_f32 v181, v181, 0, v234
	v_floor_f32_e32 v173, v173
	v_add_f32_e32 v180, 0x41000000, v180
	v_floor_f32_e32 v182, v182
	v_add_f32_e32 v169, 0x41000000, v169
	v_or3_b32 v166, v167, v166, v168
	v_mul_f32_e32 v168, v218, v229
	v_floor_f32_e32 v175, v175
	v_mul_f32_e32 v176, v220, v229
	v_cvt_i32_f32_sdwa v181, v181 dst_sel:BYTE_3 dst_unused:UNUSED_PAD src0_sel:DWORD
	v_add_f32_e32 v173, 0x41000000, v173
	v_med3_f32 v180, v180, 0, v234
	v_add_f32_e32 v182, 0x41000000, v182
	v_med3_f32 v169, v169, 0, v234
	v_floor_f32_e32 v168, v168
	v_add_f32_e32 v175, 0x41000000, v175
	v_floor_f32_e32 v176, v176
	v_med3_f32 v173, v173, 0, v234
	v_cvt_i32_f32_e32 v180, v180
	v_med3_f32 v182, v182, 0, v234
	v_cvt_i32_f32_sdwa v169, v169 dst_sel:BYTE_3 dst_unused:UNUSED_PAD src0_sel:DWORD
	v_add_f32_e32 v168, 0x41000000, v168
	v_med3_f32 v175, v175, 0, v234
	v_add_f32_e32 v176, 0x41000000, v176
	v_cvt_i32_f32_e32 v173, v173
	v_cvt_i32_f32_sdwa v182, v182 dst_sel:WORD_1 dst_unused:UNUSED_PAD src0_sel:DWORD
	v_med3_f32 v168, v168, 0, v234
	v_cvt_i32_f32_e32 v175, v175
	v_med3_f32 v176, v176, 0, v234
	v_cvt_i32_f32_e32 v168, v168
	v_cvt_i32_f32_sdwa v176, v176 dst_sel:WORD_1 dst_unused:UNUSED_PAD src0_sel:DWORD
	v_or_b32_e32 v172, v171, v181
	v_bitop3_b32 v171, v171, s77, v181 bitop3:0x36
	v_cndmask_b32_e64 v171, v171, v172, s[86:87]
	v_lshlrev_b32_e32 v172, 8, v180
	v_or_b32_e32 v167, v166, v169
	v_bitop3_b32 v166, v166, s77, v169 bitop3:0x36
	v_or3_b32 v172, v172, v173, v182
	v_mul_f32_e32 v173, v213, v229
	v_mul_f32_e32 v181, v199, v229
	v_cndmask_b32_e64 v166, v166, v167, s[86:87]
	v_lshlrev_b32_e32 v167, 8, v175
	v_floor_f32_e32 v173, v173
	v_mul_f32_e32 v180, v198, v229
	v_floor_f32_e32 v181, v181
	v_mul_f32_e32 v182, v200, v229
	v_or3_b32 v167, v167, v168, v176
	v_mul_f32_e32 v168, v221, v229
	v_mul_f32_e32 v175, v215, v229
	v_add_f32_e32 v173, 0x41000000, v173
	v_floor_f32_e32 v180, v180
	v_add_f32_e32 v181, 0x41000000, v181
	v_floor_f32_e32 v182, v182
	v_mul_f32_e32 v183, v201, v229
	v_floor_f32_e32 v168, v168
	v_mul_f32_e32 v169, v214, v229
	v_floor_f32_e32 v175, v175
	v_mul_f32_e32 v176, v216, v229
	v_med3_f32 v173, v173, 0, v234
	v_add_f32_e32 v180, 0x41000000, v180
	v_med3_f32 v181, v181, 0, v234
	v_add_f32_e32 v182, 0x41000000, v182
	v_floor_f32_e32 v183, v183
	v_add_f32_e32 v168, 0x41000000, v168
	v_floor_f32_e32 v169, v169
	v_add_f32_e32 v175, 0x41000000, v175
	v_floor_f32_e32 v176, v176
	v_cvt_i32_f32_sdwa v173, v173 dst_sel:BYTE_3 dst_unused:UNUSED_PAD src0_sel:DWORD
	v_med3_f32 v180, v180, 0, v234
	v_cvt_i32_f32_e32 v181, v181
	v_med3_f32 v182, v182, 0, v234
	v_add_f32_e32 v183, 0x41000000, v183
	v_med3_f32 v168, v168, 0, v234
	v_add_f32_e32 v169, 0x41000000, v169
	v_med3_f32 v175, v175, 0, v234
	v_add_f32_e32 v176, 0x41000000, v176
	v_cvt_i32_f32_e32 v180, v180
	v_cvt_i32_f32_sdwa v182, v182 dst_sel:WORD_1 dst_unused:UNUSED_PAD src0_sel:DWORD
	v_med3_f32 v183, v183, 0, v234
	v_cvt_i32_f32_sdwa v168, v168 dst_sel:BYTE_3 dst_unused:UNUSED_PAD src0_sel:DWORD
	v_med3_f32 v169, v169, 0, v234
	v_cvt_i32_f32_e32 v175, v175
	v_med3_f32 v176, v176, 0, v234
	v_cvt_i32_f32_sdwa v183, v183 dst_sel:BYTE_3 dst_unused:UNUSED_PAD src0_sel:DWORD
	v_cvt_i32_f32_e32 v169, v169
	v_cvt_i32_f32_sdwa v176, v176 dst_sel:WORD_1 dst_unused:UNUSED_PAD src0_sel:DWORD
	v_bitop3_b32 v172, v172, s77, v173 bitop3:0x36
	v_lshlrev_b32_e32 v173, 8, v181
	v_or3_b32 v173, v173, v180, v182
	v_mul_f32_e32 v177, v217, v229
	v_bitop3_b32 v167, v167, s77, v168 bitop3:0x36
	v_lshlrev_b32_e32 v168, 8, v175
	v_or_b32_e32 v180, v173, v183
	v_bitop3_b32 v173, v173, s77, v183 bitop3:0x36
	v_floor_f32_e32 v177, v177
	v_or3_b32 v168, v168, v169, v176
	v_mul_f32_e32 v176, v203, v229
	v_cndmask_b32_e64 v173, v173, v180, s[86:87]
	v_add_f32_e32 v177, 0x41000000, v177
	v_mul_f32_e32 v175, v202, v229
	v_floor_f32_e32 v176, v176
	v_mul_f32_e32 v180, v204, v229
	v_med3_f32 v177, v177, 0, v234
	v_floor_f32_e32 v175, v175
	v_add_f32_e32 v176, 0x41000000, v176
	v_floor_f32_e32 v180, v180
	v_cvt_i32_f32_sdwa v177, v177 dst_sel:BYTE_3 dst_unused:UNUSED_PAD src0_sel:DWORD
	v_add_f32_e32 v175, 0x41000000, v175
	v_med3_f32 v176, v176, 0, v234
	v_add_f32_e32 v180, 0x41000000, v180
	v_med3_f32 v175, v175, 0, v234
	v_cvt_i32_f32_e32 v176, v176
	v_med3_f32 v180, v180, 0, v234
	v_cvt_i32_f32_e32 v175, v175
	v_cvt_i32_f32_sdwa v180, v180 dst_sel:WORD_1 dst_unused:UNUSED_PAD src0_sel:DWORD
	v_mul_f32_e32 v191, v191, v229
	v_mul_f32_e32 v190, v190, v229
	v_floor_f32_e32 v191, v191
	v_mul_f32_e32 v192, v192, v229
	v_or_b32_e32 v169, v168, v177
	v_bitop3_b32 v168, v168, s77, v177 bitop3:0x36
	v_floor_f32_e32 v190, v190
	v_add_f32_e32 v191, 0x41000000, v191
	v_floor_f32_e32 v192, v192
	v_cndmask_b32_e64 v168, v168, v169, s[86:87]
	v_lshlrev_b32_e32 v169, 8, v176
	v_add_f32_e32 v190, 0x41000000, v190
	v_med3_f32 v191, v191, 0, v234
	v_add_f32_e32 v192, 0x41000000, v192
	v_or3_b32 v169, v169, v175, v180
	v_mul_f32_e32 v175, v205, v229
	v_mul_f32_e32 v177, v195, v229
	v_med3_f32 v190, v190, 0, v234
	v_cvt_i32_f32_e32 v191, v191
	v_med3_f32 v192, v192, 0, v234
	v_floor_f32_e32 v175, v175
	v_mul_f32_e32 v176, v194, v229
	v_floor_f32_e32 v177, v177
	v_mul_f32_e32 v180, v196, v229
	v_mul_f32_e32 v163, v163, v229
	v_cvt_i32_f32_e32 v190, v190
	v_cvt_i32_f32_sdwa v192, v192 dst_sel:WORD_1 dst_unused:UNUSED_PAD src0_sel:DWORD
	v_add_f32_e32 v175, 0x41000000, v175
	v_floor_f32_e32 v176, v176
	v_add_f32_e32 v177, 0x41000000, v177
	v_floor_f32_e32 v180, v180
	v_mul_f32_e32 v181, v197, v229
	v_mul_f32_e32 v162, v162, v229
	v_floor_f32_e32 v163, v163
	v_mul_f32_e32 v164, v164, v229
	v_mul_f32_e32 v207, v207, v229
	v_med3_f32 v175, v175, 0, v234
	v_add_f32_e32 v176, 0x41000000, v176
	v_med3_f32 v177, v177, 0, v234
	v_add_f32_e32 v180, 0x41000000, v180
	v_floor_f32_e32 v181, v181
	v_floor_f32_e32 v162, v162
	v_add_f32_e32 v163, 0x41000000, v163
	v_floor_f32_e32 v164, v164
	v_mul_f32_e32 v165, v165, v229
	v_mul_f32_e32 v206, v206, v229
	v_floor_f32_e32 v207, v207
	v_mul_f32_e32 v208, v208, v229
	v_cvt_i32_f32_sdwa v175, v175 dst_sel:BYTE_3 dst_unused:UNUSED_PAD src0_sel:DWORD
	v_med3_f32 v176, v176, 0, v234
	v_cvt_i32_f32_e32 v177, v177
	v_med3_f32 v180, v180, 0, v234
	v_add_f32_e32 v181, 0x41000000, v181
	v_add_f32_e32 v162, 0x41000000, v162
	v_med3_f32 v163, v163, 0, v234
	v_add_f32_e32 v164, 0x41000000, v164
	v_floor_f32_e32 v165, v165
	v_floor_f32_e32 v206, v206
	v_add_f32_e32 v207, 0x41000000, v207
	v_floor_f32_e32 v208, v208
	v_mul_f32_e32 v209, v209, v229
	v_lshlrev_b32_e32 v191, 8, v191
	v_mul_f32_e32 v187, v187, v229
	v_cvt_i32_f32_e32 v176, v176
	v_cvt_i32_f32_sdwa v180, v180 dst_sel:WORD_1 dst_unused:UNUSED_PAD src0_sel:DWORD
	v_med3_f32 v181, v181, 0, v234
	v_med3_f32 v162, v162, 0, v234
	v_cvt_i32_f32_e32 v163, v163
	v_med3_f32 v164, v164, 0, v234
	v_add_f32_e32 v165, 0x41000000, v165
	v_add_f32_e32 v206, 0x41000000, v206
	v_med3_f32 v207, v207, 0, v234
	v_add_f32_e32 v208, 0x41000000, v208
	v_floor_f32_e32 v209, v209
	v_or3_b32 v190, v191, v190, v192
	v_mul_f32_e32 v191, v193, v229
	v_mul_f32_e32 v186, v186, v229
	v_floor_f32_e32 v187, v187
	v_mul_f32_e32 v188, v188, v229
	v_cvt_i32_f32_sdwa v181, v181 dst_sel:BYTE_3 dst_unused:UNUSED_PAD src0_sel:DWORD
	v_cvt_i32_f32_e32 v162, v162
	v_cvt_i32_f32_sdwa v164, v164 dst_sel:WORD_1 dst_unused:UNUSED_PAD src0_sel:DWORD
	v_med3_f32 v165, v165, 0, v234
	v_med3_f32 v206, v206, 0, v234
	v_cvt_i32_f32_e32 v207, v207
	v_med3_f32 v208, v208, 0, v234
	v_add_f32_e32 v209, 0x41000000, v209
	v_floor_f32_e32 v191, v191
	v_floor_f32_e32 v186, v186
	v_add_f32_e32 v187, 0x41000000, v187
	v_floor_f32_e32 v188, v188
	v_mul_f32_e32 v189, v189, v229
	v_cvt_i32_f32_sdwa v165, v165 dst_sel:BYTE_3 dst_unused:UNUSED_PAD src0_sel:DWORD
	v_cvt_i32_f32_e32 v206, v206
	v_cvt_i32_f32_sdwa v208, v208 dst_sel:WORD_1 dst_unused:UNUSED_PAD src0_sel:DWORD
	v_med3_f32 v209, v209, 0, v234
	v_add_f32_e32 v191, 0x41000000, v191
	v_add_f32_e32 v186, 0x41000000, v186
	v_med3_f32 v187, v187, 0, v234
	v_add_f32_e32 v188, 0x41000000, v188
	v_floor_f32_e32 v189, v189
	v_bitop3_b32 v169, v169, s77, v175 bitop3:0x36
	v_lshlrev_b32_e32 v175, 8, v177
	v_cvt_i32_f32_sdwa v209, v209 dst_sel:BYTE_3 dst_unused:UNUSED_PAD src0_sel:DWORD
	v_med3_f32 v191, v191, 0, v234
	v_med3_f32 v186, v186, 0, v234
	v_cvt_i32_f32_e32 v187, v187
	v_med3_f32 v188, v188, 0, v234
	v_add_f32_e32 v189, 0x41000000, v189
	v_or3_b32 v175, v175, v176, v180
	v_lshlrev_b32_e32 v163, 8, v163
	v_cvt_i32_f32_sdwa v191, v191 dst_sel:BYTE_3 dst_unused:UNUSED_PAD src0_sel:DWORD
	v_cvt_i32_f32_e32 v186, v186
	v_cvt_i32_f32_sdwa v188, v188 dst_sel:WORD_1 dst_unused:UNUSED_PAD src0_sel:DWORD
	v_med3_f32 v189, v189, 0, v234
	v_or_b32_e32 v176, v175, v181
	v_bitop3_b32 v175, v175, s77, v181 bitop3:0x36
	v_or3_b32 v162, v163, v162, v164
	v_lshlrev_b32_e32 v207, 8, v207
	v_cvt_i32_f32_sdwa v189, v189 dst_sel:BYTE_3 dst_unused:UNUSED_PAD src0_sel:DWORD
	v_cndmask_b32_e64 v175, v175, v176, s[86:87]
	v_bitop3_b32 v176, v162, s77, v165 bitop3:0x36
	v_mov_b32_e32 v162, s61
	v_mov_b32_e32 v163, s69
	v_or3_b32 v206, v207, v206, v208
	v_cndmask_b32_e64 v163, v162, v163, s[86:87]
	v_mov_b32_e32 v162, s60
	v_mov_b32_e32 v164, s68
	v_or_b32_e32 v207, v206, v209
	v_bitop3_b32 v206, v206, s77, v209 bitop3:0x36
	v_lshlrev_b32_e32 v187, 8, v187
	v_cndmask_b32_e64 v162, v162, v164, s[86:87]
	v_lshlrev_b64 v[164:165], 8, v[230:231]
	v_cndmask_b32_e64 v206, v206, v207, s[86:87]
	v_bitop3_b32 v190, v190, s77, v191 bitop3:0x36
	v_or3_b32 v186, v187, v186, v188
	v_lshl_add_u64 v[162:163], v[162:163], 0, v[164:165]
	v_mov_b32_e32 v229, v227
	v_or_b32_e32 v187, v186, v189
	v_bitop3_b32 v186, v186, s77, v189 bitop3:0x36
	v_lshl_add_u64 v[162:163], v[162:163], 0, v[228:229]
	v_lshl_or_b32 v164, v190, 4, v206
	v_cndmask_b32_e64 v186, v186, v187, s[86:87]
	global_store_dword v[162:163], v164, off
	v_add_co_u32_e32 v164, vcc, s78, v162
	v_lshl_or_b32 v177, v178, 4, v186
	s_nop 0
	v_addc_co_u32_e32 v165, vcc, 0, v163, vcc
	global_store_dword v[164:165], v177, off
	v_add_co_u32_e32 v164, vcc, s79, v162
	v_lshl_or_b32 v170, v170, 4, v179
	s_nop 0
	v_addc_co_u32_e32 v165, vcc, 0, v163, vcc
	global_store_dword v[164:165], v170, off
	v_add_co_u32_e32 v164, vcc, s80, v162
	v_lshl_or_b32 v170, v172, 4, v171
	s_nop 0
	v_addc_co_u32_e32 v165, vcc, 0, v163, vcc
	global_store_dword v[164:165], v170, off
	v_add_co_u32_e32 v164, vcc, s81, v162
	v_lshl_or_b32 v170, v174, 4, v173
	s_nop 0
	v_addc_co_u32_e32 v165, vcc, 0, v163, vcc
	global_store_dword v[164:165], v170, off
	v_add_co_u32_e32 v164, vcc, 0x1400000, v162
	v_lshl_or_b32 v166, v167, 4, v166
	s_nop 0
	v_addc_co_u32_e32 v165, vcc, 0, v163, vcc
	global_store_dword v[164:165], v166, off
	v_add_co_u32_e32 v164, vcc, 0x1800000, v162
	v_lshl_or_b32 v166, v169, 4, v168
	s_nop 0
	v_addc_co_u32_e32 v165, vcc, 0, v163, vcc
	v_add_co_u32_e32 v162, vcc, 0x1c00000, v162
	global_store_dword v[164:165], v166, off
	v_lshl_or_b32 v164, v176, 4, v175
	v_addc_co_u32_e32 v163, vcc, 0, v163, vcc
	global_store_dword v[162:163], v164, off
	s_and_saveexec_b64 s[88:89], s[82:83]
	s_cbranch_execz .Luvh_skip_scale
	v_mov_b32_e32 v162, s67
	v_mov_b32_e32 v163, s71
	v_cndmask_b32_e64 v163, v162, v163, s[86:87]
	v_mov_b32_e32 v162, s66
	v_mov_b32_e32 v164, s70
	v_cndmask_b32_e64 v162, v162, v164, s[86:87]
	v_lshl_add_u64 v[162:163], v[230:231], 2, v[162:163]
	global_store_dword v[162:163], v235, off
.Luvh_skip_scale:
	s_or_b64 exec, exec, s[88:89]
	s_waitcnt vmcnt(9)
	ds_write_b128 v76, v[2:5]
	s_waitcnt vmcnt(8)
	ds_write_b128 v76, v[6:9] offset:16
	s_cmpk_ge_u32 s47, 0xe0
	s_cbranch_scc1 .Luvh_noload
	s_add_i32 s60, s47, 32
	s_lshr_b32 s60, s60, 5
	s_lshl_b32 s61, s2, 3
	s_add_i32 s60, s60, s61
	s_addk_i32 s60, 0x800
	v_mov_b32_e32 v162, s60
	s_mov_b64 s[62:63], s[94:95]
	s_mov_b64 s[64:65], s[94:95]
	s_movk_i32 s72, 0x1000
	s_movk_i32 s73, 0x3fff
	s_movk_i32 s74, 0x2000
	s_movk_i32 s75, 0x3000
	v_lshl_add_u32 v162, v162, 3, v232
	v_add_u32_e32 v163, 0xffffc000, v162
	v_cmp_lt_i32_e64 s[86:87], s73, v162
	v_mov_b32_e32 v164, s64
	s_nop 0
	v_cndmask_b32_e64 v230, v162, v163, s[86:87]
	v_mov_b32_e32 v162, s63
	v_mov_b32_e32 v163, s65
	v_cndmask_b32_e64 v163, v162, v163, s[86:87]
	v_mov_b32_e32 v162, s62
	v_ashrrev_i32_e32 v231, 31, v230
	v_cndmask_b32_e64 v162, v162, v164, s[86:87]
	v_lshlrev_b64 v[164:165], 14, v[230:231]
	v_lshl_add_u64 v[162:163], v[162:163], 0, v[164:165]
	v_lshl_add_u64 v[162:163], v[162:163], 0, v[226:227]
	v_add_co_u32_e32 v194, vcc, s74, v162
	global_load_dwordx4 v[206:209], v[162:163], off
	global_load_dwordx4 v[190:193], v[162:163], off offset:1024
	global_load_dwordx4 v[186:189], v[162:163], off offset:2048
	global_load_dwordx4 v[178:181], v[162:163], off offset:3072
	v_addc_co_u32_e32 v195, vcc, 0, v163, vcc
	global_load_dwordx4 v[182:185], v[194:195], off offset:-4096
	v_add_co_u32_e32 v164, vcc, s72, v162
	s_nop 0
	s_nop 0
	v_addc_co_u32_e32 v165, vcc, 0, v163, vcc
	global_load_dwordx4 v[170:173], v[164:165], off offset:1024
	v_add_co_u32_e32 v196, vcc, s75, v162
	s_nop 0
	s_nop 0
	v_addc_co_u32_e32 v197, vcc, 0, v163, vcc
	global_load_dwordx4 v[222:225], v[164:165], off offset:2048
	global_load_dwordx4 v[210:213], v[164:165], off offset:3072
	global_load_dwordx4 v[198:201], v[194:195], off
	global_load_dwordx4 v[174:177], v[194:195], off offset:1024
	global_load_dwordx4 v[166:169], v[194:195], off offset:2048
	s_nop 0
	global_load_dwordx4 v[162:165], v[196:197], off offset:3072
	global_load_dwordx4 v[86:89], v[194:195], off offset:3072
	global_load_dwordx4 v[90:93], v[196:197], off
	global_load_dwordx4 v[94:97], v[196:197], off offset:1024
	global_load_dwordx4 v[98:101], v[196:197], off offset:2048
